# speedup vs baseline: 1.0177x; 1.0177x over previous
_Z11attn_kernelPKfS0_S0_PKcS2_PKDv4_jS0_S0_S0_S0_Pf:
	s_load_dwordx8 s[4:11], s[0:1], 0x0
	s_load_dwordx8 s[12:19], s[0:1], 0x20
	v_readfirstlane_b32 s20, v0
	s_bfe_u32 s28, s2, 0x10002
	s_lshr_b32 s29, s20, 6
	s_lshr_b32 s3, s20, 8
	s_bfe_u32 s30, s20, 0x20006
	s_lshr_b32 s31, s2, 3
	s_lshl_b32 s24, s28, 18
	s_waitcnt lgkmcnt(0)
	s_add_u32 s20, s10, s24
	s_addc_u32 s10, s11, 0
	s_and_b32 s21, s10, 0xffff
	s_add_u32 s24, s12, s24
	s_addc_u32 s10, s13, 0
	v_and_b32_e32 v1, 63, v0
	s_and_b32 s25, s10, 0xffff
	s_lshl_b32 s10, s30, 10
	s_lshl_b32 s38, s3, 12
	v_lshlrev_b32_e32 v2, 4, v1
	s_or_b32 s35, s10, s38
	v_lshl_or_b32 v2, s3, 17, v2
	s_cmp_lg_u32 0, -1
	v_or_b32_e32 v174, s10, v2
	s_cselect_b32 s10, 0, 0
	s_mov_b32 s36, 0
	s_mov_b32 s23, 0x20000
	s_mov_b32 s22, 0x40000
	s_add_i32 s33, s35, s10
	s_mov_b32 m0, s33
	s_nop 0
	buffer_load_dwordx4 v174, s[20:23], s36 offen lds
	s_mov_b32 s26, s22
	s_mov_b32 s27, s23
	s_add_i32 s34, s33, 0xc000
	s_mov_b32 m0, s34
	s_nop 0
	buffer_load_dwordx4 v174, s[24:27], s36 offen lds
	s_add_i32 s10, s33, 0x4000
	s_movk_i32 s37, 0x1000
	s_mov_b32 m0, s10
	s_nop 0
	buffer_load_dwordx4 v174, s[20:23], s37 offen lds
	s_add_i32 s10, s33, 0x8000
	s_movk_i32 s11, 0x2000
	s_mov_b32 m0, s10
	s_nop 0
	buffer_load_dwordx4 v174, s[20:23], s11 offen lds
	s_lshl_b32 s10, s2, 7
	s_and_b32 s10, s10, 0x380
	s_lshl_b32 s11, s31, 2
	s_add_i32 s10, s10, s11
	s_or_b32 s10, s30, s10
	v_and_b32_e32 v172, 31, v0
	v_lshl_or_b32 v140, s10, 7, v1
	v_mov_b32_e32 v141, 0
	v_lshl_add_u64 v[6:7], v[140:141], 4, s[14:15]
	v_ashrrev_i32_e32 v9, 31, v140
	v_mov_b32_e32 v8, v140
	v_lshl_or_b32 v140, s10, 5, v172
	v_lshlrev_b64 v[4:5], 2, v[140:141]
	v_lshl_add_u64 v[2:3], s[16:17], 0, v[4:5]
	global_load_dword v2, v[2:3], off
	v_lshl_add_u64 v[8:9], v[8:9], 4, s[14:15]
	global_load_dwordx4 v[116:119], v[6:7], off
	global_load_dwordx4 v[120:123], v[8:9], off offset:1024
	s_load_dwordx4 s[12:15], s[0:1], 0x40
	s_load_dwordx2 s[10:11], s[0:1], 0x50
	v_lshlrev_b32_e32 v173, 2, v1
	v_lshl_or_b32 v3, s28, 11, v173
	s_waitcnt lgkmcnt(0)
	global_load_dword v44, v3, s[14:15] offset:256
	global_load_dword v45, v3, s[14:15]
	v_bfe_u32 v175, v0, 5, 1
	v_lshlrev_b32_e32 v0, 11, v175
	v_lshlrev_b32_e32 v3, 4, v172
	s_add_i32 s0, s38, 0
	v_lshl_add_u64 v[4:5], s[12:13], 0, v[4:5]
	v_add3_u32 v176, s0, v0, v3
	global_load_dword v0, v[4:5], off
	v_lshrrev_b32_e32 v124, 2, v1
	v_lshrrev_b32_e32 v125, 4, v1
	v_xor_b32_e32 v124, v124, v125
	v_and_b32_e32 v124, 1, v124
	v_add_u32_e32 v124, -1, v124
	v_and_b32_e32 v124, 0x38383838, v124
	v_mov_b32_e32 v200, 0
	v_mov_b32_e32 v201, 0
	v_mov_b32_e32 v202, 0
	v_mov_b32_e32 v203, 0
	v_mov_b32_e32 v204, 0
	v_mov_b32_e32 v125, v124
	v_mov_b32_e32 v126, v124
	v_mov_b32_e32 v127, v124
	v_mov_b32_e32 v128, v124
	v_mov_b32_e32 v129, v124
	v_mov_b32_e32 v130, v124
	v_mov_b32_e32 v131, v124
	v_mov_b32_e32 v140, 0x7f7f7f7f
	s_mov_b32 s0, 0xf800000
	s_movk_i32 s15, 0x3000
	s_mov_b32 s12, 1
	s_movk_i32 s14, 0x4000
	s_mov_b32 s13, 0x8000
	v_mov_b32_e32 v132, v141
	v_mov_b32_e32 v133, v141
	v_mov_b32_e32 v134, v141
	v_mov_b32_e32 v135, v141
	v_mov_b32_e32 v136, v141
	v_mov_b32_e32 v137, v141
	v_mov_b32_e32 v138, v141
	v_mov_b32_e32 v139, v141
	s_waitcnt vmcnt(5)
	v_mov_b32_e32 v4, v2
	v_mov_b32_e32 v5, v2
	v_mov_b32_e32 v6, v2
	v_mov_b32_e32 v7, v2
	v_mov_b32_e32 v8, v2
	v_mov_b32_e32 v9, v2
	v_mov_b32_e32 v10, v2
	v_mov_b32_e32 v11, v2
	v_mov_b32_e32 v12, v2
	v_mov_b32_e32 v13, v2
	v_mov_b32_e32 v14, v2
	v_mov_b32_e32 v15, v2
	v_mov_b32_e32 v16, v2
	v_mov_b32_e32 v17, v2
	v_mov_b32_e32 v3, v2
	v_mov_b64_e32 v[18:19], v[16:17]
	v_mov_b64_e32 v[16:17], v[14:15]
	v_mov_b64_e32 v[14:15], v[12:13]
	v_mov_b64_e32 v[12:13], v[10:11]
	v_mov_b64_e32 v[10:11], v[8:9]
	v_mov_b64_e32 v[8:9], v[6:7]
	v_mov_b64_e32 v[6:7], v[4:5]
	v_mov_b64_e32 v[4:5], v[2:3]
	s_waitcnt vmcnt(0) lgkmcnt(0)
	s_barrier
	ds_read_b128 v[24:27], v176 offset:1024
	ds_read_b128 v[20:23], v176
	ds_read_b128 v[36:39], v176 offset:512
	ds_read_b128 v[40:43], v176 offset:1536
	ds_read_b128 v[84:87], v176 offset:16384
	ds_read_b128 v[92:95], v176 offset:16896
	ds_read_b128 v[88:91], v176 offset:17408
	ds_read_b128 v[96:99], v176 offset:17920
	s_waitcnt vmcnt(3) lgkmcnt(6)
	v_mfma_f32_32x32x64_f8f6f4 v[20:35], v[20:27], v[116:123], v[4:19]
	s_waitcnt vmcnt(2)
	v_max_f32_e32 v3, v44, v44
	s_waitcnt vmcnt(1)
	v_max_f32_e32 v44, v45, v45
	v_max_f32_e32 v44, v44, v3
	s_nop 1
	v_max_f32_dpp v44, v44, v44 quad_perm:[1,0,3,2] row_mask:0xf bank_mask:0xf
	s_nop 1
	v_max_f32_dpp v44, v44, v44 quad_perm:[2,3,0,1] row_mask:0xf bank_mask:0xf
	s_nop 1
	v_max_f32_dpp v44, v44, v44 row_half_mirror row_mask:0xf bank_mask:0xf
	s_nop 1
	v_max_f32_dpp v44, v44, v44 row_mirror row_mask:0xf bank_mask:0xf
	s_nop 1
	v_max_f32_dpp v44, v44, v44 row_bcast:15 row_mask:0xa bank_mask:0xf
	s_nop 1
	v_max_f32_dpp v44, v44, v44 row_bcast:31 row_mask:0xc bank_mask:0xf
	s_nop 1
	v_readlane_b32 s47, v44, 63
	s_waitcnt vmcnt(0) lgkmcnt(0)
	s_barrier
	v_mfma_f32_32x32x64_f8f6f4 v[4:19], v[36:43], v[116:123], v[4:19]
	s_mov_b32 m0, s33
	s_nop 0
	buffer_load_dwordx4 v174, s[20:23], s15 offen lds
	s_add_i32 s15, s34, 0x4000
	s_mov_b32 m0, s15
	s_nop 0
	buffer_load_dwordx4 v174, s[24:27], s37 offen lds
	s_nop 1
	v_max_f32_e32 v3, v21, v21
	v_max_f32_e32 v36, v20, v20
	v_max_f32_e32 v3, v36, v3
	s_nop 7
	v_max3_f32 v37, v22, v23, v5
	v_max3_f32 v36, v37, v26, v27
	v_max3_f32 v3, v3, v4, v6
	v_max3_f32 v3, v3, v7, v24
	v_max3_f32 v36, v36, v10, v11
	v_max3_f32 v3, v3, v25, v8
	v_max3_f32 v36, v36, v30, v31
	v_max3_f32 v3, v3, v9, v28
	v_max3_f32 v36, v36, v14, v15
	v_max3_f32 v3, v3, v29, v12
	v_max3_f32 v36, v36, v34, v35
	v_max3_f32 v3, v3, v13, v32
	v_max3_f32 v36, v36, v18, v19
	v_max3_f32 v3, v3, v33, v16
	v_max3_f32 v3, v3, v17, v36
	v_mov_b32_e32 v36, v3
	s_nop 1
	v_permlane32_swap_b32_e32 v3, v36
	v_max_f32_e32 v36, v36, v36
	v_max_f32_e32 v3, v3, v3
	v_max_f32_e32 v3, v3, v36
	v_sub_f32_e32 v36, 0xc0400000, v3
	v_add_f32_e32 v20, v36, v20
	v_add_f32_e32 v21, v36, v21
	v_add_f32_e32 v22, v36, v22
	v_add_f32_e32 v23, v36, v23
	v_add_f32_e32 v24, v36, v24
	v_add_f32_e32 v25, v36, v25
	v_add_f32_e32 v26, v36, v26
	v_add_f32_e32 v27, v36, v27
	v_add_f32_e32 v28, v36, v28
	v_add_f32_e32 v29, v36, v29
	v_mov_b32_e32 v37, s47
	v_mul_f32_e32 v38, 0x4f800000, v37
	v_cmp_gt_f32_e32 vcc, s0, v37
	v_add_f32_e32 v30, v36, v30
	v_add_f32_e32 v31, v36, v31
	v_cndmask_b32_e32 v37, v37, v38, vcc
	v_sqrt_f32_e32 v38, v37
	v_add_f32_e32 v32, v36, v32
	v_add_f32_e32 v33, v36, v33
	v_add_f32_e32 v34, v36, v34
	v_add_f32_e32 v35, v36, v35
	v_add_f32_e32 v4, v36, v4
	v_add_f32_e32 v5, v36, v5
	v_add_f32_e32 v6, v36, v6
	v_add_f32_e32 v7, v36, v7
	v_add_f32_e32 v8, v36, v8
	v_add_f32_e32 v9, v36, v9
	v_add_f32_e32 v10, v36, v10
	v_add_f32_e32 v11, v36, v11
	v_add_f32_e32 v12, v36, v12
	v_add_f32_e32 v13, v36, v13
	v_add_f32_e32 v14, v36, v14
	v_add_f32_e32 v15, v36, v15
	v_add_f32_e32 v16, v36, v16
	v_add_f32_e32 v17, v36, v17
	v_add_f32_e32 v18, v36, v18
	v_add_f32_e32 v19, v36, v19
	v_add_u32_e32 v36, -1, v38
	v_fma_f32 v39, -v36, v38, v37
	v_cmp_ge_f32_e64 s[0:1], 0, v39
	v_add_u32_e32 v39, 1, v38
	v_exp_f32_e32 v161, v20
	v_cndmask_b32_e64 v36, v38, v36, s[0:1]
	v_fma_f32 v38, -v39, v38, v37
	v_cmp_lt_f32_e64 s[0:1], 0, v38
	v_exp_f32_e32 v100, v4
	v_exp_f32_e32 v163, v21
	v_cndmask_b32_e64 v36, v36, v39, s[0:1]
	v_mul_f32_e32 v38, 0x37800000, v36
	v_cndmask_b32_e32 v36, v36, v38, vcc
	v_mov_b32_e32 v38, 0x260
	v_cmp_class_f32_e32 vcc, v37, v38
	s_mov_b32 s0, 0x42700000
	v_exp_f32_e32 v148, v5
	v_cndmask_b32_e32 v36, v36, v37, vcc
	s_waitcnt vmcnt(0)
	v_mul_f32_e32 v0, v36, v0
	v_mul_f32_e32 v0, 0x3f91eb85, v0
	v_exp_f32_e32 v162, v22
	v_exp_f32_e32 v101, v6
	v_exp_f32_e32 v164, v23
	v_exp_f32_e32 v102, v7
	v_exp_f32_e32 v150, v24
	v_exp_f32_e32 v143, v8
	v_exp_f32_e32 v154, v25
	v_exp_f32_e32 v146, v9
	v_exp_f32_e32 v152, v26
	v_exp_f32_e32 v145, v10
	v_exp_f32_e32 v157, v27
	v_exp_f32_e32 v147, v11
	v_exp_f32_e32 v149, v28
	v_exp_f32_e32 v69, v12
	v_exp_f32_e32 v153, v29
	v_exp_f32_e32 v109, v13
	v_exp_f32_e32 v151, v30
	v_exp_f32_e32 v108, v14
	v_exp_f32_e32 v156, v31
	v_exp_f32_e32 v142, v15
	v_exp_f32_e32 v155, v32
	v_exp_f32_e32 v110, v16
	v_exp_f32_e32 v159, v33
	v_exp_f32_e32 v144, v17
	v_exp_f32_e32 v158, v34
	v_exp_f32_e32 v111, v18
	v_exp_f32_e32 v160, v35
	v_exp_f32_e32 v114, v19
	v_cmp_nge_f32_e64 s[0:1], s0, v0
	v_sub_f32_e32 v0, v2, v3
	v_add_f32_e32 v36, 0xc0400000, v0
	v_mov_b32_e32 v37, v36
	v_mov_b32_e32 v38, v36
	v_mov_b32_e32 v39, v36
	v_mov_b32_e32 v40, v36
	v_mov_b32_e32 v41, v36
	v_mov_b32_e32 v42, v36
	v_mov_b32_e32 v43, v36
	v_mov_b32_e32 v44, v36
	v_mov_b32_e32 v45, v36
	v_mov_b32_e32 v46, v36
	v_mov_b32_e32 v47, v36
	v_mov_b32_e32 v48, v36
	v_mov_b32_e32 v49, v36
	v_mov_b32_e32 v50, v36
	v_mov_b32_e32 v51, v36
	v_mov_b32_e32 v4, v141
	v_mov_b32_e32 v5, v141
	v_mov_b32_e32 v6, v141
	v_mov_b32_e32 v7, v141
	v_mov_b32_e32 v8, v141
	v_mov_b32_e32 v9, v141
	v_mov_b32_e32 v10, v141
	v_mov_b32_e32 v11, v141
	v_mov_b32_e32 v12, v141
	v_mov_b32_e32 v13, v141
	v_mov_b32_e32 v14, v141
	v_mov_b32_e32 v15, v141
	v_mov_b32_e32 v16, v141
	v_mov_b32_e32 v17, v141
	v_mov_b32_e32 v18, v141
	v_mov_b32_e32 v19, v141
	v_mov_b32_e32 v20, v141
	v_mov_b32_e32 v21, v141
	v_mov_b32_e32 v22, v141
	v_mov_b32_e32 v23, v141
	v_mov_b32_e32 v24, v141
	v_mov_b32_e32 v25, v141
	v_mov_b32_e32 v26, v141
	v_mov_b32_e32 v27, v141
	v_mov_b32_e32 v28, v141
	v_mov_b32_e32 v29, v141
	v_mov_b32_e32 v30, v141
	v_mov_b32_e32 v31, v141
	v_mov_b32_e32 v32, v141
	v_mov_b32_e32 v33, v141
	v_mov_b32_e32 v34, v141
	v_mov_b32_e32 v35, v141
	v_mov_b32_e32 v0, v141

	.amdhsa_kernel _Z11attn_kernelPKfS0_S0_PKcS2_PKDv4_jS0_S0_S0_S0_Pf
		.amdhsa_group_segment_fixed_size 0
		.amdhsa_private_segment_fixed_size 0
		.amdhsa_kernarg_size 88
		.amdhsa_user_sgpr_count 2
		.amdhsa_user_sgpr_dispatch_ptr 0
		.amdhsa_user_sgpr_queue_ptr 0
		.amdhsa_user_sgpr_kernarg_segment_ptr 1
		.amdhsa_user_sgpr_dispatch_id 0
		.amdhsa_user_sgpr_kernarg_preload_length 0
		.amdhsa_user_sgpr_kernarg_preload_offset 0
		.amdhsa_user_sgpr_private_segment_size 0
		.amdhsa_uses_dynamic_stack 0
		.amdhsa_enable_private_segment 0
		.amdhsa_system_sgpr_workgroup_id_x 1
		.amdhsa_system_sgpr_workgroup_id_y 0
		.amdhsa_system_sgpr_workgroup_id_z 0
		.amdhsa_system_sgpr_workgroup_info 0
		.amdhsa_system_vgpr_workitem_id 0
		.amdhsa_next_free_vgpr 256
		.amdhsa_next_free_sgpr 48
		.amdhsa_accum_offset 256
		.amdhsa_reserve_vcc 1
		.amdhsa_float_round_mode_32 0
		.amdhsa_float_round_mode_16_64 0
		.amdhsa_float_denorm_mode_32 3
		.amdhsa_float_denorm_mode_16_64 3
		.amdhsa_dx10_clamp 1
		.amdhsa_ieee_mode 1
		.amdhsa_fp16_overflow 0
		.amdhsa_tg_split 0
		.amdhsa_exception_fp_ieee_invalid_op 0
		.amdhsa_exception_fp_denorm_src 0
		.amdhsa_exception_fp_ieee_div_zero 0
		.amdhsa_exception_fp_ieee_overflow 0
		.amdhsa_exception_fp_ieee_underflow 0
		.amdhsa_exception_fp_ieee_inexact 0
		.amdhsa_exception_int_div_zero 0
	.end_amdhsa_kernel
